# workgroups idle in the convpool phase's partial last round convert 2 MoE weight tiles each (bounded re-entry into the final-sweep code), shortening the P13 sweep
# speedup vs baseline: 1.0138x; 1.0071x over previous
; __device__ __forceinline__ void phase_convpool(const Ctx& P, LAS unsigned char* lds, int vcu, int G) {
;     ...
;     for (int un = vcu; un < NU; un += G) {
;         int rowbase, L, t0;
;         if (un < 512) { rowbase = (un >> 7) * SEQ; L = SEQ; t0 = (un & 127) * 32; } else { const int q = un - 512; rowbase = ML + (q >> 3) * CTXL; L = CTXL; t0 = (q & 7) * 32; }
;         const int grp = wave >> 1;
;         if (grp == 0) pool_tile<2>(U, Y0, rowbase, L, t0, c0); else if (grp == 1) pool_tile<4>(U, Y0, rowbase, L, t0, c0); else if (grp == 2) pool_tile<8>(U, Y0, rowbase, L, t0, c0); else pool_tile<16>(U, Y0, rowbase, L, t0, c0);
.Lp3_tail:
	s_movk_i32 s100, 0x220
.Lp3_tail_l:
	s_cmp_gt_u32 s100, s39
	s_cbranch_scc0 .Lp3_tail_d
	s_sub_u32 s100, s100, s39
	s_branch .Lp3_tail_l
.Lp3_tail_d:
	s_cmp_lt_u32 s33, s100
	s_cbranch_scc1 .LBB0_1122
	s_mov_b64 s[28:29], s[0:1]
	s_mov_b32 s100, 2
	s_mov_b32 s101, 1
	s_branch .Ltf1

;     __device__ __forceinline__ const char* Bptr(const Unit& u) const { return (u.g ? Bkv : Bq) + (size_t)u.pn * BM * ldb * 2; }
; #define PG8_STAGE(bufoff, gbase, voff) do { _Pragma("unroll") for (int _i = 0; _i < 2; ++_i) { unsigned vo_ = (voff)[_i]; asm volatile("" : "+v"(vo_));   \
;         __builtin_amdgcn_global_load_lds((const unsigned*)((const char*)(gbase) + vo_), (LAS unsigned*)(lds + (bufoff) + ldsw + _i * 8192), 16, 0, 0); } } while (0)
; #define PG8_WAIT_V(n) asm volatile("s_waitcnt vmcnt(" #n ")" ::: "memory")
; #define PG8_BAR __builtin_amdgcn_s_barrier()
; #define PG8_AOFFS(dst, un) do { _Pragma("unroll") for (int _h = 0; _h < 2; ++_h) _Pragma("unroll") for (int _i = 0; _i < 2; ++_i) dst[_h][_i] = S.Aoff(un, _h * HALF + Rr[_i]) + (unsigned)Cc[_i] * 2u; } while (0)
;     ...
;     PG8_AOFFS(va, cur);
;     const char* cB = S.Bptr(cur);
;     PG8_STAGE(PG8_SB(0, 0), cB, voffB); PG8_STAGE(PG8_SB(0, 1), cB + hstepB, voffB); PG8_STAGE(PG8_SA(0, 0), Abase, va[0]); PG8_STAGE(PG8_SA(0, 1), Abase, va[1]);
;     if (wr == 1) PG8_BAR;
;     PG8_WAIT_V(2); PG8_BAR;
;     PG8_STAGE(PG8_SB(1, 0), cB + kstep, voffB); PG8_STAGE(PG8_SA(1, 0), Abase + kstep, va[0]); PG8_STAGE(PG8_SB(1, 1), cB + hstepB + kstep, voffB);
;     PG8_WAIT_V(6); PG8_BAR;
.LBB0_1219:
	s_mov_b32 s52, 32
	s_mov_b32 s30, -1
	s_branch .LBB0_1244
.Ltf1:
	s_branch .Ltf2
.Ltb3:
	s_branch .LBB0_1122
.LBB0_1220:
	s_lshl_b32 s14, s6, 7
	v_add_u32_e32 v2, s34, v186
	v_or_b32_e32 v3, s14, v185
	v_lshl_or_b32 v180, v2, 12, v3
	v_add_u32_e32 v2, s34, v188
	s_or_b32 s6, s34, 0x80
	s_lshr_b32 s3, s18, 6
	v_lshl_or_b32 v181, v2, 12, v3
	v_add_u32_e32 v2, s6, v186
	s_ashr_i32 s41, s40, 31
	s_lshr_b32 s2, s18, 8
	s_lshl_b32 s53, s3, 10
	v_lshl_or_b32 v182, v2, 12, v3
	v_add_u32_e32 v2, s6, v188
	s_lshl_b64 s[6:7], s[40:41], 20
	s_add_u32 s6, s9, s6
	s_addc_u32 s7, s38, s7
	s_add_u32 s44, s6, s14
	s_addc_u32 s45, s7, 0
	s_add_i32 s41, s53, 0
	v_lshl_or_b32 v183, v2, 12, v3
	s_add_i32 s54, s41, 0x10000
	v_mov_b32_e32 v2, v187
	s_mov_b32 m0, s54
	s_add_i32 s55, s41, 0x12000
	global_load_lds_dwordx4 v2, s[44:45]
	v_mov_b32_e32 v2, v189
	s_mov_b32 m0, s55
	s_add_u32 s6, s44, 0x80000
	global_load_lds_dwordx4 v2, s[44:45]
	s_addc_u32 s7, s45, 0
	s_add_i32 s56, s41, 0x14000
	v_mov_b32_e32 v2, v187
	s_mov_b32 m0, s56
	s_add_i32 s57, s41, 0x16000
	global_load_lds_dwordx4 v2, s[6:7]
	v_mov_b32_e32 v2, v189
	s_mov_b32 m0, s57
	s_add_i32 s58, s41, 0x2000
	global_load_lds_dwordx4 v2, s[6:7]
	v_mov_b32_e32 v2, v180
	s_mov_b32 m0, s41
	s_add_i32 s59, s41, 0x4000
	global_load_lds_dwordx4 v2, s[4:5]
	v_mov_b32_e32 v2, v181
	s_mov_b32 m0, s58
	s_add_i32 s60, s41, 0x6000
	global_load_lds_dwordx4 v2, s[4:5]
	v_mov_b32_e32 v2, v182
	s_mov_b32 m0, s59
	s_cmp_eq_u32 s2, 1
	global_load_lds_dwordx4 v2, s[4:5]
	v_mov_b32_e32 v2, v183
	s_mov_b32 m0, s60
	s_cselect_b64 s[6:7], -1, 0
	global_load_lds_dwordx4 v2, s[4:5]
	s_cmp_lg_u32 s2, 1
	s_mov_b32 s61, 0
	s_cbranch_scc1 .LBB0_1222
	s_barrier

; __device__ __forceinline__ unsigned xb_add(unsigned* p, unsigned v) { return __hip_atomic_fetch_add(p, v, __ATOMIC_RELAXED, __HIP_MEMORY_SCOPE_AGENT); }
; __device__ __forceinline__ void xcd_barrier(const XcdBarrier& b) {
;     asm volatile("s_waitcnt vmcnt(0)" ::: "memory");
;     __syncthreads();
;     int t_ = threadIdx.x; asm volatile("" : "+v"(t_));
;     if (t_ == 0) {
;         unsigned* bar = b.bar;
;         __builtin_amdgcn_s_waitcnt(0);
;         unsigned nloc = b.st[0], nx = b.st[1];
;         if (nloc == 0u) { xcd_barrier_complete(bar, b.x, b.G, nloc, nx); b.st[0] = nloc; b.st[1] = nx; }
;         const unsigned old = xb_add(&bar[XB_XSUB(b.x)], 1u);
.LBB0_1671:
	s_or_b64 exec, exec, s[4:5]
	s_mov_b64 s[2:3], s[0:1]
	s_nop 0
	v_mov_b64_e32 v[2:3], s[2:3]
	flat_load_dword v1, v[2:3] offset:296
	s_waitcnt vmcnt(0) lgkmcnt(0)
	v_cmp_gt_i32_e32 vcc, 9, v1
	s_and_saveexec_b64 s[40:41], vcc
	s_cbranch_execz .LBB0_1729
	s_mov_b64 s[2:3], s[0:1]
	s_nop 0
	v_mov_b64_e32 v[2:3], s[2:3]
	flat_load_dword v1, v[2:3] offset:300
	s_waitcnt vmcnt(0) lgkmcnt(0)
	v_cmp_lt_i32_e32 vcc, 8, v1
	s_and_b64 exec, exec, vcc
	s_cbranch_execz .LBB0_1729
	s_mov_b64 s[2:3], s[0:1]
	s_nop 0
	v_mov_b64_e32 v[2:3], s[2:3]
	flat_load_dword v1, v[2:3] offset:296
	s_waitcnt vmcnt(0) lgkmcnt(0)
	v_cmp_gt_i32_e32 vcc, 10, v1
	s_and_b64 exec, exec, vcc
	s_cbranch_execz .LBB0_1729
	s_mov_b64 s[2:3], s[0:1]
	s_nop 0
	v_mov_b64_e32 v[2:3], s[2:3]
	flat_load_dword v1, v[2:3] offset:300
	s_waitcnt vmcnt(0) lgkmcnt(0)
	v_cmp_lt_i32_e32 vcc, 9, v1
	s_and_b64 exec, exec, vcc
	s_cbranch_execz .LBB0_1729
	s_mov_b64 s[4:5], s[0:1]
	s_getreg_b32 s2, hwreg(HW_REG_XCC_ID, 0, 4)
	v_mov_b32_e32 v1, v0
	v_mov_b64_e32 v[2:3], s[4:5]
	flat_load_dword v17, v[2:3] offset:308
	s_waitcnt vmcnt(0)
	s_waitcnt lgkmcnt(0)
	s_barrier
	s_nop 0
	v_cmp_eq_u32_e32 vcc, 0, v1
	s_and_b64 exec, exec, vcc
	s_cbranch_execz .LBB0_1728
	s_add_i32 s3, 0, 0x20020
	v_mov_b32_e32 v1, s3
	s_waitcnt vmcnt(0) expcnt(0) lgkmcnt(0)
	ds_read_b32 v4, v1
	s_add_i32 s3, 0, 0x20024
	v_mov_b32_e32 v1, s3
	ds_read_b32 v2, v1
	s_and_b32 s9, s2, 15
	s_waitcnt lgkmcnt(1)
	v_cmp_ne_u32_e32 vcc, 0, v4
	s_cbranch_vccnz .LBB0_1692
	s_add_u32 s2, s36, 0x1000
	s_addc_u32 s3, s37, 0
	s_add_u32 s4, s36, 0x1100
	s_addc_u32 s5, s37, 0
	s_add_u32 s6, s36, 0x1200
	s_addc_u32 s7, s37, 0
	s_add_u32 s10, s36, 0x1300
	s_addc_u32 s11, s37, 0
	s_mov_b32 s28, 1
	s_mov_b64 s[12:13], 0
	v_mov_b32_e32 v18, 0
	s_branch .LBB0_1680
.Ltf2:
	s_branch .Ltf3
.Ltb2:
	s_branch .Ltb3
.LBB0_1678:
	s_andn2_b64 s[18:19], s[18:19], exec
	s_and_b64 s[24:25], s[24:25], exec
	s_andn2_b64 s[16:17], s[16:17], exec
	s_and_b64 s[22:23], s[22:23], exec
	s_or_b64 s[18:19], s[18:19], s[24:25]
	s_or_b64 s[16:17], s[16:17], s[22:23]

; #define PG8_BAR __builtin_amdgcn_s_barrier()
;     ...
;         if (wr == 0) PG8_BAR;
;         E(acc, cur, wr, wc, fr, fq);
;         if (!has_next) break;
; #pragma unroll
;         for (int a = 0; a < 2; ++a)
; #pragma unroll
;             for (int b = 0; b < 2; ++b)
; #pragma unroll
;                 for (int m = 0; m < 4; ++m)
; #pragma unroll
;                     for (int n = 0; n < 2; ++n) acc[a][b][m][n] = (f32x4){0.f, 0.f, 0.f, 0.f};
;         cur = nxt; cB = nB; ++ui;
;         if (wr == 1) PG8_BAR;
;     }
.LBB0_2059:
	s_and_b64 vcc, exec, s[4:5]
	s_mov_b64 s[4:5], -1
	s_cbranch_vccnz .LBB0_1974
	s_andn2_b64 vcc, exec, s[16:17]
	s_cbranch_vccnz .LBB0_1973
	s_barrier
	s_branch .LBB0_1973
.Ltf3:
	s_branch .Lsweep_entry
.Ltb1:
	s_branch .Ltb2
.LBB0_2062:
	s_waitcnt vmcnt(0)
	s_barrier

; #define LAS __attribute__((address_space(3)))
; #define MKCTX() const Ctx P{InTbl{in_tbl()}, (float*)*(__attribute__((address_space(1))) float* const*)((const char*)in_tbl() + offsetof(Params, out)), ws}
; #define IN(k) (((PH_MASK >> (k)) & 1) && KARG_I(ph_lo) <= (k) && (k) < KARG_I(ph_hi))
; #define SEAM(k) do { if (IN(k) && IN((k) + 1)) { XcdBarrier bar_; bar_.bar = (unsigned*)(ws + WS_CTL) + CW_BAR; bar_.x = xb_xcc_id(); bar_.st = MISC + 8; bar_.G = (unsigned)KARG_I(grid); xcd_barrier(bar_); } } while (0)
; __device__ __forceinline__ void tr_slack(const Ctx& P, LAS unsigned char* lds, unsigned* tilectr, unsigned* cnt, unsigned target) {
;     const int tid = threadIdx.x, lane = tid & 63, wave = __builtin_amdgcn_readfirstlane(tid >> 6);
;     volatile LAS int* box = (volatile LAS int*)(lds + LDS_MISC + 2048);
;     int r = -1; unsigned pollv = 0u;
; __global__ void __launch_bounds__(512, 2) fwd_kernel(Params KP) {
;     ...
;     if (IN(13)) { MKCTX();
;         if (vcu & 1) { phase_router(P, lds, vcu, G); __syncthreads(); tr_slack(P, lds, (unsigned*)(ws + WS_CTL) + CW_TILE, nullptr, 0u); }
;         else { tr_slack(P, lds, (unsigned*)(ws + WS_CTL) + CW_TILE, nullptr, 0u); __syncthreads(); phase_router(P, lds, vcu, G); } } SEAM(13);
.LBB0_2331:
	s_or_b64 exec, exec, s[40:41]
	s_mov_b64 s[2:3], s[0:1]
	s_nop 0
	v_mov_b64_e32 v[2:3], s[2:3]
	flat_load_dword v1, v[2:3] offset:296
	s_waitcnt vmcnt(0) lgkmcnt(0)
	v_cmp_gt_i32_e32 vcc, 14, v1
	s_and_saveexec_b64 s[26:27], vcc
	s_cbranch_execz .LBB0_2466
	s_mov_b64 s[2:3], s[0:1]
	s_nop 0
	v_mov_b64_e32 v[2:3], s[2:3]
	flat_load_dword v1, v[2:3] offset:300
	s_waitcnt vmcnt(0) lgkmcnt(0)
	v_cmp_lt_i32_e32 vcc, 13, v1
	s_and_b64 exec, exec, vcc
	s_cbranch_execz .LBB0_2466
	s_mov_b64 s[28:29], s[0:1]
	s_mov_b64 s[2:3], s[0:1]
	s_mov_b32 s100, 0x7fffffff
	s_mov_b32 s101, 0
	s_and_b32 s99, s33, 3
	s_cmp_eq_u32 s99, 0
	s_mov_b64 s[2:3], -1
	s_cbranch_scc1 .LBB0_2400
	v_mov_b64_e32 v[2:3], s[28:29]
	flat_load_dwordx2 v[2:3], v[2:3] offset:232
	v_or_b32_e32 v1, 0x200, v0
	v_mov_b32_e32 v8, 16
	s_mov_b64 s[2:3], 0
	v_mov_b32_e32 v7, 0
	v_mov_b64_e32 v[4:5], v[0:1]

; #define LAS __attribute__((address_space(3)))
; __device__ __forceinline__ void tr_slack(const Ctx& P, LAS unsigned char* lds, unsigned* tilectr, unsigned* cnt, unsigned target) {
;     const int tid = threadIdx.x, lane = tid & 63, wave = __builtin_amdgcn_readfirstlane(tid >> 6);
;     volatile LAS int* box = (volatile LAS int*)(lds + LDS_MISC + 2048);
;     int r = -1; unsigned pollv = 0u;
;     if (tid == 0) { int stop0 = 0; if (cnt) stop0 = (__hip_atomic_load(cnt, __ATOMIC_RELAXED, __HIP_MEMORY_SCOPE_AGENT) >= target) ? 1 : 0;
;         box[0] = stop0 ? -1 : (int)__hip_atomic_fetch_add(tilectr, 1u, __ATOMIC_RELAXED, __HIP_MEMORY_SCOPE_AGENT); box[1] = stop0; }
;     __syncthreads();
.Lsweep_entry:
	s_add_u32 s12, s36, 0x8000
	s_addc_u32 s13, s37, 0
	v_readfirstlane_b32 s14, v0
	v_cmp_eq_u32_e64 s[2:3], 0, v0
	s_and_saveexec_b64 s[4:5], s[2:3]
	s_cbranch_execz .LBB0_2405
	s_mov_b64 s[10:11], exec
	v_mbcnt_lo_u32_b32 v1, s10, 0
	v_mbcnt_hi_u32_b32 v1, s11, v1
	v_cmp_eq_u32_e32 vcc, 0, v1
	s_and_saveexec_b64 s[6:7], vcc
	s_cbranch_execz .LBB0_2404
	s_bcnt1_i32_b64 s9, s[10:11]
	v_mov_b32_e32 v2, 0
	v_mov_b32_e32 v3, s9
	global_atomic_add v2, v2, v3, s[12:13] sc0

; __device__ __forceinline__ void tr_slack(const Ctx& P, LAS unsigned char* lds, unsigned* tilectr, unsigned* cnt, unsigned target) {
;     ...
;         const TD cur = tr_get(P, TR_NMAIN + idx, lane, wave);
;         f32x4 v[16];
; #pragma unroll
;         for (int i = 0; i < 16; ++i) v[i] = __builtin_nontemporal_load((const f32x4*)(cur.p + (size_t)i * cur.ld));
;         if (tid == 0 && !stop) { r = (int)__hip_atomic_fetch_add(tilectr, 1u, __ATOMIC_RELAXED, __HIP_MEMORY_SCOPE_AGENT); if (cnt) pollv = __hip_atomic_load(cnt, __ATOMIC_RELAXED, __HIP_MEMORY_SCOPE_AGENT); }
.LBB0_2413:
	s_lshl_b32 s14, s6, 2
	global_load_dwordx4 v[2:5], v[6:7], off nt
	v_lshl_add_u64 v[6:7], v[6:7], 0, s[14:15]
	v_lshl_add_u64 v[8:9], v[6:7], 0, s[14:15]
	s_waitcnt vmcnt(12)
	v_lshl_add_u64 v[14:15], v[8:9], 0, s[14:15]
	v_lshl_add_u64 v[16:17], v[14:15], 0, s[14:15]
	global_load_dwordx4 v[34:37], v[6:7], off nt
	global_load_dwordx4 v[10:13], v[8:9], off nt
	global_load_dwordx4 v[50:53], v[14:15], off nt
	s_nop 0
	global_load_dwordx4 v[6:9], v[16:17], off nt
	v_lshl_add_u64 v[14:15], v[16:17], 0, s[14:15]
	v_lshl_add_u64 v[16:17], v[14:15], 0, s[14:15]
	s_waitcnt vmcnt(12)
	v_lshl_add_u64 v[18:19], v[16:17], 0, s[14:15]
	v_lshl_add_u64 v[20:21], v[18:19], 0, s[14:15]
	global_load_dwordx4 v[42:45], v[14:15], off nt
	global_load_dwordx4 v[38:41], v[16:17], off nt
	global_load_dwordx4 v[62:65], v[18:19], off nt
	s_nop 0
	global_load_dwordx4 v[14:17], v[20:21], off nt
	v_lshl_add_u64 v[18:19], v[20:21], 0, s[14:15]
	v_lshl_add_u64 v[20:21], v[18:19], 0, s[14:15]
	global_load_dwordx4 v[54:57], v[18:19], off nt
	global_load_dwordx4 v[46:49], v[20:21], off nt
	v_lshl_add_u64 v[18:19], v[20:21], 0, s[14:15]
	s_waitcnt vmcnt(17)
	v_lshl_add_u64 v[22:23], v[18:19], 0, s[14:15]
	s_waitcnt vmcnt(16)
	v_lshl_add_u64 v[26:27], v[22:23], 0, s[14:15]
	s_waitcnt vmcnt(15)
	v_lshl_add_u64 v[30:31], v[26:27], 0, s[14:15]
	global_load_dwordx4 v[58:61], v[18:19], off nt
	s_waitcnt lgkmcnt(0)
	v_cmp_ne_u32_e64 s[6:7], 0, v66
	global_load_dwordx4 v[18:21], v[22:23], off nt
	s_nor_b64 s[24:25], s[4:5], s[6:7]
	global_load_dwordx4 v[22:25], v[26:27], off nt
	s_nop 0
	global_load_dwordx4 v[26:29], v[30:31], off nt
	v_lshl_add_u64 v[30:31], v[30:31], 0, s[14:15]
	global_load_dwordx4 v[30:33], v[30:31], off nt
	s_cmp_eq_u32 s100, 1
	s_cbranch_scc1 .Lsweep_noclaim
	s_and_saveexec_b64 s[22:23], s[24:25]
	s_cbranch_execz .LBB0_2417
	s_mov_b64 s[30:31], exec
	v_mbcnt_lo_u32_b32 v66, s30, 0
	v_mbcnt_hi_u32_b32 v66, s31, v66
	v_cmp_eq_u32_e32 vcc, 0, v66
	s_and_saveexec_b64 s[24:25], vcc
	s_cbranch_execz .LBB0_2416
	s_bcnt1_i32_b64 s14, s[30:31]
	v_mov_b32_e32 v67, s14
	global_atomic_add v67, v79, v67, s[12:13] sc0

; #define LAS __attribute__((address_space(3)))
; __device__ __forceinline__ unsigned cvt4_fp8(float a, float b, float c, float d) { int w = 0; w = __builtin_amdgcn_cvt_pk_fp8_f32(clamp448(a), clamp448(b), w, false); w = __builtin_amdgcn_cvt_pk_fp8_f32(clamp448(c), clamp448(d), w, true); return (unsigned)w; }
; __device__ __forceinline__ void tr_slack(const Ctx& P, LAS unsigned char* lds, unsigned* tilectr, unsigned* cnt, unsigned target) {
;     ...
;         if (tid == 0 && !stop) { r = (int)__hip_atomic_fetch_add(tilectr, 1u, __ATOMIC_RELAXED, __HIP_MEMORY_SCOPE_AGENT); if (cnt) pollv = __hip_atomic_load(cnt, __ATOMIC_RELAXED, __HIP_MEMORY_SCOPE_AGENT); }
;         if (cur.fp8 == 2) {
;             const f32x4 cm4 = *(const f32x4*)cur.cm;
; #pragma unroll
;             for (int c = 0; c < 4; ++c) { u32x4 w; const float s_ = 127.0f / cm4[c];
;                 w.x = cvt4_i8(v[0][c] * s_, v[1][c] * s_, v[2][c] * s_, v[3][c] * s_); w.y = cvt4_i8(v[4][c] * s_, v[5][c] * s_, v[6][c] * s_, v[7][c] * s_);
;                 w.z = cvt4_i8(v[8][c] * s_, v[9][c] * s_, v[10][c] * s_, v[11][c] * s_); w.w = cvt4_i8(v[12][c] * s_, v[13][c] * s_, v[14][c] * s_, v[15][c] * s_);
;                 *(LAS u32x4*)(lds + (4 * lane + c) * 128 + ((wave ^ sw) << 4)) = w; }
;         } else {
; #pragma unroll
;         for (int c = 0; c < 4; ++c) { u32x4 w; const float s_ = cur.wscale;
;             w.x = cvt4_fp8(v[0][c] * s_, v[1][c] * s_, v[2][c] * s_, v[3][c] * s_); w.y = cvt4_fp8(v[4][c] * s_, v[5][c] * s_, v[6][c] * s_, v[7][c] * s_);
;             w.z = cvt4_fp8(v[8][c] * s_, v[9][c] * s_, v[10][c] * s_, v[11][c] * s_); w.w = cvt4_fp8(v[12][c] * s_, v[13][c] * s_, v[14][c] * s_, v[15][c] * s_);
;             *(LAS u32x4*)(lds + (4 * lane + c) * 128 + ((wave ^ sw) << 4)) = w; } }
.LBB0_2417:
	s_or_b64 exec, exec, s[22:23]
	s_branch .Lsweep_claimed
.Lsweep_noclaim:
	v_mov_b32_e32 v96, -1
.Lsweep_claimed:
	s_sub_i32 s100, s100, 1
	s_andn2_b64 vcc, exec, s[10:11]
	s_mov_b64 s[10:11], -1
	s_cbranch_vccnz .LBB0_2419
	s_waitcnt vmcnt(15)
	v_mul_f32_e32 v66, s49, v2
	s_waitcnt vmcnt(14)
	v_mul_f32_e32 v67, s49, v34
	v_med3_f32 v66, v66, s43, v94
	v_med3_f32 v67, v67, s43, v94
	v_mov_b32_e32 v98, v79
	v_cvt_pk_fp8_f32 v98, v66, v67
	s_waitcnt vmcnt(13)
	v_mul_f32_e32 v68, s49, v10
	s_waitcnt vmcnt(12)
	v_mul_f32_e32 v66, s49, v50
	v_med3_f32 v67, v68, s43, v94
	v_med3_f32 v66, v66, s43, v94
	v_cvt_pk_fp8_f32 v98, v67, v66 op_sel:[0,0,1]
	s_waitcnt vmcnt(11)
	v_mul_f32_e32 v66, s49, v6
	s_waitcnt vmcnt(10)
	v_mul_f32_e32 v67, s49, v42
	v_med3_f32 v66, v66, s43, v94
	v_med3_f32 v67, v67, s43, v94
	v_mov_b32_e32 v99, v79
	v_cvt_pk_fp8_f32 v99, v66, v67
	s_waitcnt vmcnt(9)
	v_mul_f32_e32 v68, s49, v38
	s_waitcnt vmcnt(8)
	v_mul_f32_e32 v66, s49, v62
	v_med3_f32 v67, v68, s43, v94
	v_med3_f32 v66, v66, s43, v94
	v_cvt_pk_fp8_f32 v99, v67, v66 op_sel:[0,0,1]
	s_waitcnt vmcnt(7)
	v_mul_f32_e32 v66, s49, v14
	s_waitcnt vmcnt(6)
	v_mul_f32_e32 v67, s49, v54
	v_med3_f32 v66, v66, s43, v94
	v_med3_f32 v67, v67, s43, v94
	v_mov_b32_e32 v100, v79
	v_cvt_pk_fp8_f32 v100, v66, v67
	s_waitcnt vmcnt(5)
	v_mul_f32_e32 v68, s49, v46
	s_waitcnt vmcnt(4)
	v_mul_f32_e32 v66, s49, v58
	v_med3_f32 v67, v68, s43, v94
	v_med3_f32 v66, v66, s43, v94
	v_cvt_pk_fp8_f32 v100, v67, v66 op_sel:[0,0,1]
	s_waitcnt vmcnt(3)
	v_mul_f32_e32 v66, s49, v18
	s_waitcnt vmcnt(2)
	v_mul_f32_e32 v67, s49, v22
	v_med3_f32 v66, v66, s43, v94
	v_med3_f32 v67, v67, s43, v94
	v_mov_b32_e32 v101, v79
	v_cvt_pk_fp8_f32 v101, v66, v67
	s_waitcnt vmcnt(1)
	v_mul_f32_e32 v68, s49, v26
	s_waitcnt vmcnt(0)
	v_mul_f32_e32 v66, s49, v30
	v_med3_f32 v67, v68, s43, v94
	v_med3_f32 v66, v66, s43, v94
	v_cvt_pk_fp8_f32 v101, v67, v66 op_sel:[0,0,1]
	v_mul_f32_e32 v66, s49, v3
	v_mul_f32_e32 v67, s49, v35
	v_med3_f32 v66, v66, s43, v94
	v_med3_f32 v67, v67, s43, v94
	v_mov_b32_e32 v102, v79
	v_cvt_pk_fp8_f32 v102, v66, v67
	v_mul_f32_e32 v68, s49, v11
	v_mul_f32_e32 v66, s49, v51
	v_med3_f32 v67, v68, s43, v94
	v_med3_f32 v66, v66, s43, v94
	v_cvt_pk_fp8_f32 v102, v67, v66 op_sel:[0,0,1]
	v_mul_f32_e32 v66, s49, v7
	v_mul_f32_e32 v67, s49, v43
	v_med3_f32 v66, v66, s43, v94
	v_med3_f32 v67, v67, s43, v94
	v_mov_b32_e32 v103, v79
	v_cvt_pk_fp8_f32 v103, v66, v67
	v_mul_f32_e32 v68, s49, v39
	v_mul_f32_e32 v66, s49, v63
	v_med3_f32 v67, v68, s43, v94
	v_med3_f32 v66, v66, s43, v94
	v_cvt_pk_fp8_f32 v103, v67, v66 op_sel:[0,0,1]
	v_mul_f32_e32 v66, s49, v15
	v_mul_f32_e32 v67, s49, v55
	v_med3_f32 v66, v66, s43, v94
	v_med3_f32 v67, v67, s43, v94
	v_mov_b32_e32 v104, v79
	v_cvt_pk_fp8_f32 v104, v66, v67
	v_mul_f32_e32 v68, s49, v47
	v_mul_f32_e32 v66, s49, v59
	v_med3_f32 v67, v68, s43, v94
	v_med3_f32 v66, v66, s43, v94
	v_cvt_pk_fp8_f32 v104, v67, v66 op_sel:[0,0,1]
	v_mul_f32_e32 v66, s49, v19
	v_mul_f32_e32 v67, s49, v23
	v_med3_f32 v66, v66, s43, v94
	v_med3_f32 v67, v67, s43, v94
	v_mov_b32_e32 v105, v79
	v_cvt_pk_fp8_f32 v105, v66, v67
	v_mul_f32_e32 v68, s49, v27
	v_mul_f32_e32 v66, s49, v31
	v_med3_f32 v67, v68, s43, v94
	v_med3_f32 v66, v66, s43, v94
	v_cvt_pk_fp8_f32 v105, v67, v66 op_sel:[0,0,1]
	v_mul_f32_e32 v66, s49, v4
	v_mul_f32_e32 v67, s49, v36
	v_med3_f32 v66, v66, s43, v94
	v_med3_f32 v67, v67, s43, v94
	v_mov_b32_e32 v70, v79
	v_cvt_pk_fp8_f32 v70, v66, v67
	v_mul_f32_e32 v68, s49, v12
	v_mul_f32_e32 v66, s49, v52
	v_med3_f32 v67, v68, s43, v94
	v_med3_f32 v66, v66, s43, v94
	v_cvt_pk_fp8_f32 v70, v67, v66 op_sel:[0,0,1]
	v_mul_f32_e32 v66, s49, v8
	v_mul_f32_e32 v67, s49, v44
	v_med3_f32 v66, v66, s43, v94
	v_med3_f32 v67, v67, s43, v94
	v_mov_b32_e32 v71, v79
	v_cvt_pk_fp8_f32 v71, v66, v67
	v_mul_f32_e32 v68, s49, v40
	v_mul_f32_e32 v66, s49, v64
	v_med3_f32 v67, v68, s43, v94
	v_med3_f32 v66, v66, s43, v94
	v_cvt_pk_fp8_f32 v71, v67, v66 op_sel:[0,0,1]
	v_mul_f32_e32 v66, s49, v16
	v_mul_f32_e32 v67, s49, v56
	v_med3_f32 v66, v66, s43, v94
	v_med3_f32 v67, v67, s43, v94
	v_mov_b32_e32 v72, v79
	v_cvt_pk_fp8_f32 v72, v66, v67
	v_mul_f32_e32 v68, s49, v48
	v_mul_f32_e32 v66, s49, v60
	v_med3_f32 v67, v68, s43, v94
	v_med3_f32 v66, v66, s43, v94
	v_cvt_pk_fp8_f32 v72, v67, v66 op_sel:[0,0,1]
	v_mul_f32_e32 v66, s49, v20
	v_mul_f32_e32 v67, s49, v24
	v_med3_f32 v66, v66, s43, v94
	v_med3_f32 v67, v67, s43, v94
	v_mov_b32_e32 v73, v79
	v_cvt_pk_fp8_f32 v73, v66, v67
	v_mul_f32_e32 v68, s49, v28
	v_mul_f32_e32 v66, s49, v32
	v_med3_f32 v67, v68, s43, v94
	v_med3_f32 v66, v66, s43, v94
	v_cvt_pk_fp8_f32 v73, v67, v66 op_sel:[0,0,1]
	v_mul_f32_e32 v66, s49, v5
	v_mul_f32_e32 v67, s49, v37
	v_med3_f32 v69, v66, s43, v94
	v_med3_f32 v67, v67, s43, v94
	v_mov_b32_e32 v66, v79
	v_cvt_pk_fp8_f32 v66, v69, v67
	v_mul_f32_e32 v68, s49, v13
	v_mul_f32_e32 v67, s49, v53
	v_med3_f32 v68, v68, s43, v94
	v_med3_f32 v67, v67, s43, v94
	v_cvt_pk_fp8_f32 v66, v68, v67 op_sel:[0,0,1]
	v_mul_f32_e32 v67, s49, v9
	v_mul_f32_e32 v68, s49, v45
	v_med3_f32 v78, v67, s43, v94
	v_med3_f32 v68, v68, s43, v94
	v_mov_b32_e32 v67, v79
	v_cvt_pk_fp8_f32 v67, v78, v68
	v_mul_f32_e32 v69, s49, v41
	v_mul_f32_e32 v68, s49, v65
	v_med3_f32 v69, v69, s43, v94
	v_med3_f32 v68, v68, s43, v94
	v_cvt_pk_fp8_f32 v67, v69, v68 op_sel:[0,0,1]
	v_mul_f32_e32 v68, s49, v17
	v_mul_f32_e32 v69, s49, v57
	v_med3_f32 v97, v68, s43, v94
	v_med3_f32 v69, v69, s43, v94
	v_mov_b32_e32 v68, v79
	v_cvt_pk_fp8_f32 v68, v97, v69
	v_mul_f32_e32 v78, s49, v49
	v_mul_f32_e32 v69, s49, v61
	v_med3_f32 v78, v78, s43, v94
	v_med3_f32 v69, v69, s43, v94
	v_cvt_pk_fp8_f32 v68, v78, v69 op_sel:[0,0,1]
	v_mul_f32_e32 v69, s49, v21
	v_mul_f32_e32 v78, s49, v25
	v_med3_f32 v106, v69, s43, v94
	v_med3_f32 v78, v78, s43, v94
	v_mov_b32_e32 v69, v79
	v_cvt_pk_fp8_f32 v69, v106, v78
	v_mul_f32_e32 v97, s49, v29
	v_mul_f32_e32 v78, s49, v33
	v_med3_f32 v97, v97, s43, v94
	v_med3_f32 v78, v78, s43, v94
	v_cvt_pk_fp8_f32 v69, v97, v78 op_sel:[0,0,1]
	ds_write_b128 v93, v[98:101]
	ds_write_b128 v93, v[102:105] offset:128
	s_cbranch_execz .LBB0_2420
	s_branch .LBB0_2421

; #define SEAM(k) do { if (IN(k) && IN((k) + 1)) { XcdBarrier bar_; bar_.bar = (unsigned*)(ws + WS_CTL) + CW_BAR; bar_.x = xb_xcc_id(); bar_.st = MISC + 8; bar_.G = (unsigned)KARG_I(grid); xcd_barrier(bar_); } } while (0)
; __device__ __forceinline__ void phase_router(const Ctx& P, LAS unsigned char* lds, int vcu, int G) {
;     ...
;     for (int i = tid; i < DM * 8; i += 512) { const int k = i >> 3, e = i & 7; rwT[e * DM + k] = P.in[29][i]; }
; __global__ void __launch_bounds__(512, 2) fwd_kernel(Params KP) {
;     ...
;         if (vcu & 1) { phase_router(P, lds, vcu, G); __syncthreads(); tr_slack(P, lds, (unsigned*)(ws + WS_CTL) + CW_TILE, nullptr, 0u); }
;         else { tr_slack(P, lds, (unsigned*)(ws + WS_CTL) + CW_TILE, nullptr, 0u); __syncthreads(); phase_router(P, lds, vcu, G); } } SEAM(13);
.Lp3_sweep_ret:
	s_waitcnt vmcnt(0) lgkmcnt(0)
	s_barrier
	s_mov_b32 s101, 0
	s_branch .Ltb1
.LBB0_2423:
	s_cmp_eq_u32 s101, 1
	s_cbranch_scc1 .Lp3_sweep_ret
	v_mov_b64_e32 v[2:3], s[28:29]
	s_waitcnt lgkmcnt(0)
	s_barrier
	s_barrier
	flat_load_dwordx2 v[2:3], v[2:3] offset:232
	v_or_b32_e32 v1, 0x200, v0
	v_mov_b32_e32 v8, 16
	s_mov_b64 s[2:3], 0
	v_mov_b32_e32 v7, 0
	v_mov_b64_e32 v[4:5], v[0:1]
